# select row remap guarded on 256-CU grid; dsa straight-line far path kept
# speedup vs baseline: 1.0177x; 1.0000x over previous
.LBB0_603:
	s_lshl_b64 s[0:1], s[4:5], 9
	v_readlane_b32 s2, v253, 60
	s_add_u32 s0, s2, s0
	v_readlane_b32 s2, v253, 61
	s_addc_u32 s1, s2, s1
	v_lshl_add_u64 v[6:7], v[74:75], 3, s[0:1]
	v_readlane_b32 s0, v253, 57
	v_readlane_b32 s101, v252, 0
	s_nop 3
	s_cmp_lg_u32 s101, 0x100
	s_cbranch_scc1 .Lsel_remap_skip_0
	s_xor_b32 s100, s4, 0x7ff
	s_bitcmp1_b32 s4, 11
	s_cselect_b32 s4, s100, s4
.Lsel_remap_skip_0:
	s_add_i32 s4, s4, s0
	v_readlane_b32 s72, v254, 2
	s_cmpk_lt_i32 s4, 0x4000
	global_store_dwordx2 v[6:7], v[4:5], off
	s_cbranch_scc0 .LBB0_1152
.LBB0_604:
	v_readlane_b32 s101, v252, 0
	s_nop 3
	s_cmp_lg_u32 s101, 0x100
	s_cbranch_scc1 .Lsel_remap_skip_1
	s_xor_b32 s100, s4, 0x7ff
	s_bitcmp1_b32 s4, 11
	s_cselect_b32 s4, s100, s4
